# baseline (speedup 1.0000x reference)
_Z11attn_kernelPKfS0_S0_PKcS2_PKDv4_jS0_S0_S0_S0_Pf:
	s_load_dwordx8 s[4:11], s[0:1], 0x0
	s_load_dwordx8 s[12:19], s[0:1], 0x20
	v_readfirstlane_b32 s20, v0
	s_bfe_u32 s28, s2, 0x10002
	s_lshr_b32 s29, s20, 6
	s_lshr_b32 s3, s20, 8
	s_bfe_u32 s30, s20, 0x20006
	s_lshr_b32 s31, s2, 3
	s_lshl_b32 s24, s28, 18
	s_waitcnt lgkmcnt(0)
	s_add_u32 s20, s10, s24
	s_addc_u32 s10, s11, 0
	s_and_b32 s21, s10, 0xffff
	s_add_u32 s24, s12, s24
	s_addc_u32 s10, s13, 0
	v_and_b32_e32 v1, 63, v0
	s_and_b32 s25, s10, 0xffff
	s_lshl_b32 s10, s30, 10
	s_lshl_b32 s38, s3, 12
	v_lshlrev_b32_e32 v2, 4, v1
	s_or_b32 s35, s10, s38
	v_lshl_or_b32 v2, s3, 17, v2
	s_cmp_lg_u32 0, -1
	v_or_b32_e32 v174, s10, v2
	s_cselect_b32 s10, 0, 0
	s_mov_b32 s36, 0
	s_mov_b32 s23, 0x20000
	s_mov_b32 s22, 0x40000
	s_add_i32 s33, s35, s10
	s_mov_b32 m0, s33
	s_nop 0
	buffer_load_dwordx4 v174, s[20:23], s36 offen lds
	s_mov_b32 s26, s22
	s_mov_b32 s27, s23
	s_add_i32 s34, s33, 0xc000
	s_mov_b32 m0, s34
	s_nop 0
	buffer_load_dwordx4 v174, s[24:27], s36 offen lds
	s_add_i32 s10, s33, 0x4000
	s_movk_i32 s37, 0x1000
	s_mov_b32 m0, s10
	s_nop 0
	buffer_load_dwordx4 v174, s[20:23], s37 offen lds
	s_add_i32 s10, s33, 0x8000
	s_movk_i32 s11, 0x2000
	s_mov_b32 m0, s10
	s_nop 0
	buffer_load_dwordx4 v174, s[20:23], s11 offen lds
	s_lshl_b32 s10, s2, 7
	s_and_b32 s10, s10, 0x380
	s_lshl_b32 s11, s31, 2
	s_add_i32 s10, s10, s11
	s_or_b32 s10, s30, s10
	v_and_b32_e32 v172, 31, v0
	v_lshl_or_b32 v140, s10, 7, v1
	v_mov_b32_e32 v141, 0
	v_lshl_add_u64 v[6:7], v[140:141], 4, s[14:15]
	v_ashrrev_i32_e32 v9, 31, v140
	v_mov_b32_e32 v8, v140
	v_lshl_or_b32 v140, s10, 5, v172
	v_lshlrev_b64 v[4:5], 2, v[140:141]
	v_lshl_add_u64 v[2:3], s[16:17], 0, v[4:5]
	global_load_dword v2, v[2:3], off
	v_lshl_add_u64 v[8:9], v[8:9], 4, s[14:15]
	global_load_dwordx4 v[116:119], v[6:7], off
	global_load_dwordx4 v[120:123], v[8:9], off offset:1024
	s_load_dwordx4 s[12:15], s[0:1], 0x40
	s_load_dwordx2 s[10:11], s[0:1], 0x50
	v_lshlrev_b32_e32 v173, 2, v1
	v_lshl_or_b32 v3, s28, 11, v173
	s_waitcnt lgkmcnt(0)
	global_load_dword v44, v3, s[14:15] offset:256
	global_load_dword v45, v3, s[14:15]
	v_bfe_u32 v175, v0, 5, 1
	v_lshlrev_b32_e32 v0, 11, v175
	v_lshlrev_b32_e32 v3, 4, v172
	s_add_i32 s0, s38, 0
	v_lshl_add_u64 v[4:5], s[12:13], 0, v[4:5]
	v_add3_u32 v176, s0, v0, v3
	global_load_dword v0, v[4:5], off
	v_lshrrev_b32_e32 v124, 2, v1
	v_lshrrev_b32_e32 v125, 4, v1
	v_xor_b32_e32 v124, v124, v125
	v_and_b32_e32 v124, 1, v124
	v_add_u32_e32 v124, -1, v124
	v_and_b32_e32 v124, 0x38383838, v124
	v_mov_b32_e32 v200, 0
	v_mov_b32_e32 v201, 0
	v_mov_b32_e32 v202, 0
	v_mov_b32_e32 v203, 0
	v_mov_b32_e32 v204, 0
	v_mov_b32_e32 v125, v124
	v_mov_b32_e32 v126, v124
	v_mov_b32_e32 v127, v124
	v_mov_b32_e32 v128, v124
	v_mov_b32_e32 v129, v124
	v_mov_b32_e32 v130, v124
	v_mov_b32_e32 v131, v124
	v_mov_b32_e32 v140, 0x7f7f7f7f
	s_mov_b32 s0, 0xf800000
	s_movk_i32 s15, 0x3000
	s_mov_b32 s12, 1
	s_movk_i32 s14, 0x4000
	s_mov_b32 s13, 0x8000
	v_mov_b32_e32 v132, v141
	v_mov_b32_e32 v133, v141
	v_mov_b32_e32 v134, v141
	v_mov_b32_e32 v135, v141
	v_mov_b32_e32 v136, v141
	v_mov_b32_e32 v137, v141
	v_mov_b32_e32 v138, v141
	v_mov_b32_e32 v139, v141
	s_waitcnt vmcnt(5)
	v_mov_b32_e32 v4, v2
	v_mov_b32_e32 v5, v2
	v_mov_b32_e32 v6, v2
	v_mov_b32_e32 v7, v2
	v_mov_b32_e32 v8, v2
	v_mov_b32_e32 v9, v2
	v_mov_b32_e32 v10, v2
	v_mov_b32_e32 v11, v2
	v_mov_b32_e32 v12, v2
	v_mov_b32_e32 v13, v2
	v_mov_b32_e32 v14, v2
	v_mov_b32_e32 v15, v2
	v_mov_b32_e32 v16, v2
	v_mov_b32_e32 v17, v2
	v_mov_b32_e32 v3, v2
	v_mov_b64_e32 v[18:19], v[16:17]
	v_mov_b64_e32 v[16:17], v[14:15]
	v_mov_b64_e32 v[14:15], v[12:13]
	v_mov_b64_e32 v[12:13], v[10:11]
	v_mov_b64_e32 v[10:11], v[8:9]
	v_mov_b64_e32 v[8:9], v[6:7]
	v_mov_b64_e32 v[6:7], v[4:5]
	v_mov_b64_e32 v[4:5], v[2:3]
	s_waitcnt vmcnt(0) lgkmcnt(0)
	s_barrier
	ds_read_b128 v[24:27], v176 offset:1024
	ds_read_b128 v[20:23], v176
	ds_read_b128 v[36:39], v176 offset:512
	ds_read_b128 v[40:43], v176 offset:1536
	ds_read_b128 v[84:87], v176 offset:16384
	ds_read_b128 v[92:95], v176 offset:16896
	ds_read_b128 v[88:91], v176 offset:17408
	ds_read_b128 v[96:99], v176 offset:17920
	s_waitcnt vmcnt(3) lgkmcnt(6)
	v_mfma_f32_32x32x64_f8f6f4 v[20:35], v[20:27], v[116:123], v[4:19]
	v_mbcnt_lo_u32_b32 v3, -1, 0
	v_mbcnt_hi_u32_b32 v46, -1, v3
	v_and_b32_e32 v3, 64, v46
	v_xor_b32_e32 v47, 32, v46
	v_add_u32_e32 v48, 64, v3
	s_waitcnt vmcnt(2)
	v_max_f32_e32 v3, v44, v44
	s_waitcnt vmcnt(1)
	v_max_f32_e32 v44, v45, v45
	v_max_f32_e32 v44, v44, v3
	v_cmp_lt_i32_e32 vcc, v47, v48
	s_waitcnt vmcnt(0) lgkmcnt(0)
	s_barrier
	v_mfma_f32_32x32x64_f8f6f4 v[4:19], v[36:43], v[116:123], v[4:19]
	s_mov_b32 m0, s33
	s_nop 0
	buffer_load_dwordx4 v174, s[20:23], s15 offen lds
	s_add_i32 s15, s34, 0x4000
	s_mov_b32 m0, s15
	s_nop 0
	buffer_load_dwordx4 v174, s[24:27], s37 offen lds
	s_nop 1
	v_max_f32_e32 v3, v21, v21
	v_max_f32_e32 v36, v20, v20
	v_max_f32_e32 v3, v36, v3
	v_xor_b32_e32 v38, 16, v46
	s_nop 6
	v_max3_f32 v37, v22, v23, v5
	v_max3_f32 v36, v37, v26, v27
	v_cndmask_b32_e32 v37, v46, v47, vcc
	v_lshlrev_b32_e32 v37, 2, v37
	ds_bpermute_b32 v37, v37, v44
	v_cmp_lt_i32_e32 vcc, v38, v48
	v_max3_f32 v3, v3, v4, v6
	v_max3_f32 v3, v3, v7, v24
	v_cndmask_b32_e32 v38, v46, v38, vcc
	s_waitcnt lgkmcnt(0)
	v_max_f32_e32 v37, v37, v37
	v_max_f32_e32 v37, v44, v37
	v_lshlrev_b32_e32 v38, 2, v38
	ds_bpermute_b32 v38, v38, v37
	v_max3_f32 v36, v36, v10, v11
	v_max3_f32 v3, v3, v25, v8
	v_max3_f32 v36, v36, v30, v31
	v_max3_f32 v3, v3, v9, v28
	s_waitcnt lgkmcnt(0)
	v_max_f32_e32 v38, v38, v38
	v_max_f32_e32 v37, v37, v38
	v_xor_b32_e32 v38, 8, v46
	v_cmp_lt_i32_e32 vcc, v38, v48
	v_max3_f32 v36, v36, v14, v15
	v_max3_f32 v3, v3, v29, v12
	v_cndmask_b32_e32 v38, v46, v38, vcc
	v_lshlrev_b32_e32 v38, 2, v38
	ds_bpermute_b32 v38, v38, v37
	v_max3_f32 v36, v36, v34, v35
	v_max3_f32 v3, v3, v13, v32
	v_max3_f32 v36, v36, v18, v19
	v_max3_f32 v3, v3, v33, v16
	s_waitcnt lgkmcnt(0)
	v_max_f32_e32 v38, v38, v38
	v_max_f32_e32 v37, v37, v38
	v_xor_b32_e32 v38, 4, v46
	v_cmp_lt_i32_e32 vcc, v38, v48
	v_max3_f32 v3, v3, v17, v36
	v_mov_b32_e32 v36, v3
	v_cndmask_b32_e32 v38, v46, v38, vcc
	v_lshlrev_b32_e32 v38, 2, v38
	ds_bpermute_b32 v38, v38, v37
	v_permlane32_swap_b32_e32 v3, v36
	v_max_f32_e32 v36, v36, v36
	v_max_f32_e32 v3, v3, v3
	s_waitcnt lgkmcnt(0)
	v_max_f32_e32 v38, v38, v38
	v_max_f32_e32 v37, v37, v38
	v_xor_b32_e32 v38, 2, v46
	v_cmp_lt_i32_e32 vcc, v38, v48
	v_max_f32_e32 v3, v3, v36
	v_sub_f32_e32 v36, 0xc0400000, v3
	v_cndmask_b32_e32 v38, v46, v38, vcc
	v_lshlrev_b32_e32 v38, 2, v38
	ds_bpermute_b32 v38, v38, v37
	v_add_f32_e32 v20, v36, v20
	v_add_f32_e32 v21, v36, v21
	v_add_f32_e32 v22, v36, v22
	v_add_f32_e32 v23, v36, v23
	s_waitcnt lgkmcnt(0)
	v_max_f32_e32 v38, v38, v38
	v_max_f32_e32 v37, v37, v38
	v_xor_b32_e32 v38, 1, v46
	v_cmp_lt_i32_e32 vcc, v38, v48
	v_add_f32_e32 v24, v36, v24
	v_add_f32_e32 v25, v36, v25
	v_cndmask_b32_e32 v38, v46, v38, vcc
	v_lshlrev_b32_e32 v38, 2, v38
	ds_bpermute_b32 v38, v38, v37
	v_add_f32_e32 v26, v36, v26
	v_add_f32_e32 v27, v36, v27
	v_add_f32_e32 v28, v36, v28
	v_add_f32_e32 v29, v36, v29
	s_waitcnt lgkmcnt(0)
	v_max_f32_e32 v38, v38, v38
	v_max_f32_e32 v37, v37, v38
	v_mul_f32_e32 v38, 0x4f800000, v37
	v_cmp_gt_f32_e32 vcc, s0, v37
	v_add_f32_e32 v30, v36, v30
	v_add_f32_e32 v31, v36, v31
	v_cndmask_b32_e32 v37, v37, v38, vcc
	v_sqrt_f32_e32 v38, v37
	v_add_f32_e32 v32, v36, v32
	v_add_f32_e32 v33, v36, v33
	v_add_f32_e32 v34, v36, v34
	v_add_f32_e32 v35, v36, v35
	v_add_f32_e32 v4, v36, v4
	v_add_f32_e32 v5, v36, v5
	v_add_f32_e32 v6, v36, v6
	v_add_f32_e32 v7, v36, v7
	v_add_f32_e32 v8, v36, v8
	v_add_f32_e32 v9, v36, v9
	v_add_f32_e32 v10, v36, v10
	v_add_f32_e32 v11, v36, v11
	v_add_f32_e32 v12, v36, v12
	v_add_f32_e32 v13, v36, v13
	v_add_f32_e32 v14, v36, v14
	v_add_f32_e32 v15, v36, v15
	v_add_f32_e32 v16, v36, v16
	v_add_f32_e32 v17, v36, v17
	v_add_f32_e32 v18, v36, v18
	v_add_f32_e32 v19, v36, v19
	v_add_u32_e32 v36, -1, v38
	v_fma_f32 v39, -v36, v38, v37
	v_cmp_ge_f32_e64 s[0:1], 0, v39
	v_add_u32_e32 v39, 1, v38
	v_exp_f32_e32 v161, v20
	v_cndmask_b32_e64 v36, v38, v36, s[0:1]
	v_fma_f32 v38, -v39, v38, v37
	v_cmp_lt_f32_e64 s[0:1], 0, v38
	v_exp_f32_e32 v100, v4
	v_exp_f32_e32 v163, v21
	v_cndmask_b32_e64 v36, v36, v39, s[0:1]
	v_mul_f32_e32 v38, 0x37800000, v36
	v_cndmask_b32_e32 v36, v36, v38, vcc
	v_mov_b32_e32 v38, 0x260
	v_cmp_class_f32_e32 vcc, v37, v38
	s_mov_b32 s0, 0x42700000
	v_exp_f32_e32 v148, v5
	v_cndmask_b32_e32 v36, v36, v37, vcc
	s_waitcnt vmcnt(0)
	v_mul_f32_e32 v0, v36, v0
	v_mul_f32_e32 v0, 0x3f91eb85, v0
	v_exp_f32_e32 v162, v22
	v_exp_f32_e32 v101, v6
	v_exp_f32_e32 v164, v23
	v_exp_f32_e32 v102, v7
	v_exp_f32_e32 v150, v24
	v_exp_f32_e32 v143, v8
	v_exp_f32_e32 v154, v25
	v_exp_f32_e32 v146, v9
	v_exp_f32_e32 v152, v26
	v_exp_f32_e32 v145, v10
	v_exp_f32_e32 v157, v27
	v_exp_f32_e32 v147, v11
	v_exp_f32_e32 v149, v28
	v_exp_f32_e32 v69, v12
	v_exp_f32_e32 v153, v29
	v_exp_f32_e32 v109, v13
	v_exp_f32_e32 v151, v30
	v_exp_f32_e32 v108, v14
	v_exp_f32_e32 v156, v31
	v_exp_f32_e32 v142, v15
	v_exp_f32_e32 v155, v32
	v_exp_f32_e32 v110, v16
	v_exp_f32_e32 v159, v33
	v_exp_f32_e32 v144, v17
	v_exp_f32_e32 v158, v34
	v_exp_f32_e32 v111, v18
	v_exp_f32_e32 v160, v35
	v_exp_f32_e32 v114, v19
	v_cmp_nge_f32_e64 s[0:1], s0, v0
	v_sub_f32_e32 v0, v2, v3
	v_add_f32_e32 v36, 0xc0400000, v0
	v_mov_b32_e32 v37, v36
	v_mov_b32_e32 v38, v36
	v_mov_b32_e32 v39, v36
	v_mov_b32_e32 v40, v36
	v_mov_b32_e32 v41, v36
	v_mov_b32_e32 v42, v36
	v_mov_b32_e32 v43, v36
	v_mov_b32_e32 v44, v36
	v_mov_b32_e32 v45, v36
	v_mov_b32_e32 v46, v36
	v_mov_b32_e32 v47, v36
	v_mov_b32_e32 v48, v36
	v_mov_b32_e32 v49, v36
	v_mov_b32_e32 v50, v36
	v_mov_b32_e32 v51, v36
	v_mov_b32_e32 v4, v141
	v_mov_b32_e32 v5, v141
	v_mov_b32_e32 v6, v141
	v_mov_b32_e32 v7, v141
	v_mov_b32_e32 v8, v141
	v_mov_b32_e32 v9, v141
	v_mov_b32_e32 v10, v141
	v_mov_b32_e32 v11, v141
	v_mov_b32_e32 v12, v141
	v_mov_b32_e32 v13, v141
	v_mov_b32_e32 v14, v141
	v_mov_b32_e32 v15, v141
	v_mov_b32_e32 v16, v141
	v_mov_b32_e32 v17, v141
	v_mov_b32_e32 v18, v141
	v_mov_b32_e32 v19, v141
	v_mov_b32_e32 v20, v141
	v_mov_b32_e32 v21, v141
	v_mov_b32_e32 v22, v141
	v_mov_b32_e32 v23, v141
	v_mov_b32_e32 v24, v141
	v_mov_b32_e32 v25, v141
	v_mov_b32_e32 v26, v141
	v_mov_b32_e32 v27, v141
	v_mov_b32_e32 v28, v141
	v_mov_b32_e32 v29, v141
	v_mov_b32_e32 v30, v141
	v_mov_b32_e32 v31, v141
	v_mov_b32_e32 v32, v141
	v_mov_b32_e32 v33, v141
	v_mov_b32_e32 v34, v141
	v_mov_b32_e32 v35, v141
	v_mov_b32_e32 v0, v141
